# RSTAT partial-sum loop: all sixteen partial loads issued before the accumulation (registers renamed), adds keep their order
# baseline (speedup 1.0000x reference)
; __device__ __forceinline__ void ret_stats(const float* PT, float* ST, int gtid, int nthr) {
;     for (int i = gtid; i < M * 8; i += nthr) { const int hd = i / M, row = i - hd * M; const f32x2_t* p = (const f32x2_t*)PT + (size_t)hd * 16 * M + row; float sv = 0.f, sq = 0.f;
; #pragma unroll
;         for (int k = 0; k < 16; ++k) { const f32x2_t v = p[(size_t)k * M]; sv += v.x; sq += v.y; }
;         *(f32x2_t*)(ST + ((size_t)row * 8 + hd) * 2) = (f32x2_t){sv, sq}; }
; }
.LBB0_32:
	v_ashrrev_i32_e32 v1, 31, v0
	v_lshrrev_b32_e32 v1, 17, v1
	v_add_u32_e32 v1, v0, v1
	v_ashrrev_i32_e32 v8, 15, v1
	v_and_b32_e32 v10, 0xffff8000, v1
	v_ashrrev_i32_e32 v9, 31, v8
	v_ashrrev_i32_e32 v11, 31, v10
	v_lshlrev_b64 v[12:13], 22, v[8:9]
	v_lshlrev_b64 v[14:15], 3, v[10:11]
	v_sub_co_u32_e32 v12, vcc, v12, v14
	s_mov_b32 s3, 0x1da00000
	s_nop 0
	v_subb_co_u32_e32 v13, vcc, v13, v15, vcc
	v_lshl_add_u64 v[14:15], v[4:5], 0, s[10:11]
	v_lshl_add_u64 v[12:13], v[14:15], 0, v[12:13]
	v_add_co_u32_e32 v14, vcc, s3, v12
	s_mov_b32 s3, 0x1da40000
	s_nop 0
	v_addc_co_u32_e32 v15, vcc, 0, v13, vcc
	v_add_co_u32_e32 v16, vcc, s3, v12
	global_load_dwordx2 v[14:15], v[14:15], off
	s_nop 0
	v_addc_co_u32_e32 v17, vcc, 0, v13, vcc
	s_mov_b32 s3, 0x1da80000
	global_load_dwordx2 v[16:17], v[16:17], off
	v_add_co_u32_e32 v18, vcc, s3, v12
	s_mov_b32 s3, 0x1dac0000
	s_nop 0
	v_addc_co_u32_e32 v19, vcc, 0, v13, vcc
	global_load_dwordx2 v[18:19], v[18:19], off
	v_add_co_u32_e32 v20, vcc, s3, v12
	s_mov_b32 s3, 0x1db00000
	s_nop 0
	v_addc_co_u32_e32 v21, vcc, 0, v13, vcc
	global_load_dwordx2 v[20:21], v[20:21], off
	v_add_co_u32_e32 v22, vcc, s3, v12
	s_mov_b32 s3, 0x1db40000
	s_nop 0
	v_addc_co_u32_e32 v23, vcc, 0, v13, vcc
	global_load_dwordx2 v[22:23], v[22:23], off
	v_lshlrev_b64 v[8:9], 3, v[8:9]
	v_lshlrev_b64 v[10:11], 6, v[10:11]
	v_add_u32_e32 v0, s2, v0
	v_lshl_add_u64 v[4:5], v[4:5], 0, s[4:5]
	v_add_co_u32_e32 v36, vcc, s3, v12
	s_mov_b32 s3, 0x1db80000
	s_nop 0
	v_addc_co_u32_e32 v37, vcc, 0, v13, vcc
	v_add_co_u32_e32 v38, vcc, s3, v12
	s_mov_b32 s3, 0x1dbc0000
	s_nop 0
	v_addc_co_u32_e32 v39, vcc, 0, v13, vcc
	v_add_co_u32_e32 v40, vcc, s3, v12
	s_mov_b32 s3, 0x1dc00000
	s_nop 0
	v_addc_co_u32_e32 v41, vcc, 0, v13, vcc
	v_add_co_u32_e32 v42, vcc, s3, v12
	s_mov_b32 s3, 0x1dc40000
	s_nop 0
	v_addc_co_u32_e32 v43, vcc, 0, v13, vcc
	v_add_co_u32_e32 v24, vcc, s3, v12
	s_mov_b32 s3, 0x1dc80000
	s_nop 0
	v_addc_co_u32_e32 v25, vcc, 0, v13, vcc
	v_add_co_u32_e32 v26, vcc, s3, v12
	s_mov_b32 s3, 0x1dcc0000
	s_nop 0
	v_addc_co_u32_e32 v27, vcc, 0, v13, vcc
	global_load_dwordx2 v[36:37], v[36:37], off
	v_add_co_u32_e32 v28, vcc, s3, v12
	global_load_dwordx2 v[38:39], v[38:39], off
	s_nop 0
	v_addc_co_u32_e32 v29, vcc, 0, v13, vcc
	s_mov_b32 s3, 0x1dd00000
	global_load_dwordx2 v[40:41], v[40:41], off
	v_add_co_u32_e32 v30, vcc, s3, v12
	global_load_dwordx2 v[42:43], v[42:43], off
	s_nop 0
	v_addc_co_u32_e32 v31, vcc, 0, v13, vcc
	s_mov_b32 s3, 0x1dd40000
	global_load_dwordx2 v[24:25], v[24:25], off
	v_add_co_u32_e32 v32, vcc, s3, v12
	global_load_dwordx2 v[26:27], v[26:27], off
	s_nop 0
	v_addc_co_u32_e32 v33, vcc, 0, v13, vcc
	s_mov_b32 s3, 0x1dd80000
	global_load_dwordx2 v[28:29], v[28:29], off
	v_add_co_u32_e32 v34, vcc, s3, v12
	global_load_dwordx2 v[30:31], v[30:31], off
	s_nop 0
	v_addc_co_u32_e32 v35, vcc, 0, v13, vcc
	s_mov_b32 s3, 0x1ddc0000
	global_load_dwordx2 v[32:33], v[32:33], off
	v_add_co_u32_e32 v12, vcc, s3, v12
	global_load_dwordx2 v[34:35], v[34:35], off
	s_nop 0
	v_addc_co_u32_e32 v13, vcc, 0, v13, vcc
	global_load_dwordx2 v[12:13], v[12:13], off
	v_sub_co_u32_e32 v8, vcc, v8, v10
	s_mov_b32 s3, 0x3ffff
	s_nop 0
	v_subb_co_u32_e32 v9, vcc, v9, v11, vcc
	v_lshl_add_u64 v[10:11], v[6:7], 0, s[10:11]
	v_cmp_lt_i32_e32 vcc, s3, v0
	v_lshl_add_u64 v[8:9], v[10:11], 0, v[8:9]
	v_lshl_add_u64 v[6:7], v[6:7], 0, s[6:7]
	s_or_b64 s[8:9], vcc, s[8:9]
	s_waitcnt vmcnt(15)
	v_pk_add_f32 v[14:15], v[14:15], 0 op_sel_hi:[1,0]
	s_waitcnt vmcnt(14)
	v_pk_add_f32 v[14:15], v[14:15], v[16:17]
	s_waitcnt vmcnt(13)
	v_pk_add_f32 v[14:15], v[14:15], v[18:19]
	s_waitcnt vmcnt(12)
	v_pk_add_f32 v[14:15], v[14:15], v[20:21]
	s_waitcnt vmcnt(11)
	v_pk_add_f32 v[14:15], v[14:15], v[22:23]
	s_waitcnt vmcnt(10)
	v_pk_add_f32 v[14:15], v[14:15], v[36:37]
	s_waitcnt vmcnt(9)
	v_pk_add_f32 v[14:15], v[14:15], v[38:39]
	s_waitcnt vmcnt(8)
	v_pk_add_f32 v[14:15], v[14:15], v[40:41]
	s_waitcnt vmcnt(7)
	v_pk_add_f32 v[14:15], v[14:15], v[42:43]
	s_waitcnt vmcnt(6)
	v_pk_add_f32 v[14:15], v[14:15], v[24:25]
	s_waitcnt vmcnt(5)
	v_pk_add_f32 v[14:15], v[14:15], v[26:27]
	s_waitcnt vmcnt(4)
	v_pk_add_f32 v[14:15], v[14:15], v[28:29]
	s_waitcnt vmcnt(3)
	v_pk_add_f32 v[14:15], v[14:15], v[30:31]
	s_waitcnt vmcnt(2)
	v_pk_add_f32 v[14:15], v[14:15], v[32:33]
	s_waitcnt vmcnt(1)
	v_pk_add_f32 v[14:15], v[14:15], v[34:35]
	s_waitcnt vmcnt(0)
	v_pk_add_f32 v[12:13], v[14:15], v[12:13]
	global_store_dwordx2 v[8:9], v[12:13], off
	s_andn2_b64 exec, exec, s[8:9]
	s_cbranch_execnz .LBB0_32
